# P0 f32 weight loads (read once) tagged nt
# speedup vs baseline: 1.0074x; 1.0002x over previous
; template <int NCH>
; __device__ __forceinline__ void quant_colblock(const Frame& F, const float* src, int ld_src, int nvalid, unsigned char* dst, int ld_dst, float* sb) {
;     ...
; #pragma unroll
;     for (int bt = 0; bt <= 2 * NCH; ++bt) {
;         if (bt < 2 * NCH) {
; #pragma unroll
;             for (int i = 0; i < 8; ++i) vb[bt & 1][i] = *(const f32x4*)(rb + (size_t)((bt >> 1) * 128 + 8 * (bt & 1) + i) * ld_src + loff); }
;         __builtin_amdgcn_sched_barrier(0);
;         if (bt > 0) { const int pb = bt - 1, c = pb >> 1, hb = pb & 1; f32x4 (&v)[8] = vb[pb & 1]; unsigned t[8][2];
; #pragma unroll
;             for (int i = 0; i < 8; ++i) { v[i].x = ok ? v[i].x : 0.f; v[i].y = ok ? v[i].y : 0.f; v[i].z = ok ? v[i].z : 0.f; v[i].w = ok ? v[i].w : 0.f; }
; #pragma unroll
;             for (int i = 0; i < 8; ++i) { m.x = fmaxf(m.x, fabsf(v[i].x)); m.y = fmaxf(m.y, fabsf(v[i].y)); m.z = fmaxf(m.z, fabsf(v[i].z)); m.w = fmaxf(m.w, fabsf(v[i].w));
.LBB0_31:
	s_mul_hi_u32 s51, s28, s73
	s_mul_i32 s50, s28, s73
	s_lshl_b64 s[50:51], s[50:51], 2
	s_add_u32 s48, s48, s50
	v_mul_u32_u24_e32 v2, s28, v47
	s_addc_u32 s49, s49, s51
	v_or_b32_e32 v34, v2, v138
	v_lshl_add_u64 v[2:3], v[34:35], 2, s[48:49]
	v_lshl_add_u64 v[4:5], s[28:29], 2, v[2:3]
	s_lshl_b32 s48, s28, 1
	s_mov_b32 s49, s29
	global_load_dwordx4 v[6:9], v[2:3], off nt
	global_load_dwordx4 v[10:13], v[4:5], off nt
	v_lshl_add_u64 v[4:5], s[48:49], 2, v[2:3]
	s_mul_i32 s48, s28, 3
	v_lshl_add_u64 v[18:19], s[48:49], 2, v[2:3]
	s_lshl_b32 s48, s28, 2
	global_load_dwordx4 v[14:17], v[4:5], off nt
	s_nop 0
	global_load_dwordx4 v[18:21], v[18:19], off nt
	v_lshl_add_u64 v[4:5], s[48:49], 2, v[2:3]
	s_mul_i32 s48, s28, 5
	v_lshl_add_u64 v[26:27], s[48:49], 2, v[2:3]
	s_mul_i32 s48, s28, 6
	global_load_dwordx4 v[22:25], v[4:5], off nt
	s_nop 0
	global_load_dwordx4 v[26:29], v[26:27], off nt
	v_lshl_add_u64 v[4:5], s[48:49], 2, v[2:3]
	s_mul_i32 s48, s28, 7
	v_lshl_add_u64 v[38:39], s[48:49], 2, v[2:3]
	global_load_dwordx4 v[30:33], v[4:5], off nt
	s_nop 0
	global_load_dwordx4 v[38:41], v[38:39], off nt
	s_lshl_b32 s48, s28, 3
	v_lshl_add_u64 v[4:5], s[48:49], 2, v[2:3]
	s_mul_i32 s48, s28, 9
	v_lshl_add_u64 v[60:61], s[48:49], 2, v[2:3]
	s_mul_i32 s48, s28, 10
	global_load_dwordx4 v[42:45], v[4:5], off nt
	global_load_dwordx4 v[64:67], v[60:61], off nt
	v_lshl_add_u64 v[4:5], s[48:49], 2, v[2:3]
	s_mul_i32 s48, s28, 11
	v_lshl_add_u64 v[60:61], s[48:49], 2, v[2:3]
	s_mul_i32 s48, s28, 12
	global_load_dwordx4 v[68:71], v[4:5], off nt
	global_load_dwordx4 v[72:75], v[60:61], off nt
	v_lshl_add_u64 v[4:5], s[48:49], 2, v[2:3]
	s_mul_i32 s48, s28, 13
	v_lshl_add_u64 v[60:61], s[48:49], 2, v[2:3]
	s_mul_i32 s48, s28, 14
	global_load_dwordx4 v[76:79], v[4:5], off nt
	global_load_dwordx4 v[80:83], v[60:61], off nt
	v_lshl_add_u64 v[4:5], s[48:49], 2, v[2:3]
	s_mul_i32 s48, s28, 15
	v_lshl_add_u64 v[60:61], s[48:49], 2, v[2:3]
	global_load_dwordx4 v[84:87], v[4:5], off nt
	global_load_dwordx4 v[88:91], v[60:61], off nt
	s_waitcnt vmcnt(15)
	v_cndmask_b32_e64 v6, 0, v6, s[46:47]
	v_cndmask_b32_e64 v7, 0, v7, s[46:47]
	v_cndmask_b32_e64 v8, 0, v8, s[46:47]
	v_cndmask_b32_e64 v9, 0, v9, s[46:47]
	s_waitcnt vmcnt(14)
	v_cndmask_b32_e64 v10, 0, v10, s[46:47]
	v_cndmask_b32_e64 v11, 0, v11, s[46:47]
	v_cndmask_b32_e64 v12, 0, v12, s[46:47]
	v_cndmask_b32_e64 v13, 0, v13, s[46:47]
	s_waitcnt vmcnt(13)
	v_cndmask_b32_e64 v14, 0, v14, s[46:47]
	v_cndmask_b32_e64 v15, 0, v15, s[46:47]
	v_cndmask_b32_e64 v16, 0, v16, s[46:47]
	v_cndmask_b32_e64 v17, 0, v17, s[46:47]
	s_waitcnt vmcnt(12)
	v_cndmask_b32_e64 v18, 0, v18, s[46:47]
	v_cndmask_b32_e64 v19, 0, v19, s[46:47]
	v_cndmask_b32_e64 v20, 0, v20, s[46:47]
	v_cndmask_b32_e64 v21, 0, v21, s[46:47]
	v_max3_f32 v4, |v6|, 0, |v10|
	v_max3_f32 v5, |v7|, 0, |v11|
	v_max3_f32 v34, |v8|, 0, |v12|
	v_max3_f32 v60, |v9|, 0, |v13|
	s_waitcnt vmcnt(11)
	v_cndmask_b32_e64 v22, 0, v22, s[46:47]
	v_cndmask_b32_e64 v23, 0, v23, s[46:47]
	v_cndmask_b32_e64 v24, 0, v24, s[46:47]
	v_cndmask_b32_e64 v25, 0, v25, s[46:47]
	s_waitcnt vmcnt(10)
	v_cndmask_b32_e64 v26, 0, v26, s[46:47]
	v_cndmask_b32_e64 v27, 0, v27, s[46:47]
	v_cndmask_b32_e64 v28, 0, v28, s[46:47]
	v_cndmask_b32_e64 v29, 0, v29, s[46:47]
	v_max3_f32 v4, v4, |v14|, |v18|
	v_max3_f32 v5, v5, |v15|, |v19|
	v_max3_f32 v34, v34, |v16|, |v20|
	v_max3_f32 v60, v60, |v17|, |v21|
	s_waitcnt vmcnt(9)
	v_cndmask_b32_e64 v30, 0, v30, s[46:47]
	v_cndmask_b32_e64 v31, 0, v31, s[46:47]
	v_cndmask_b32_e64 v32, 0, v32, s[46:47]
	v_cndmask_b32_e64 v33, 0, v33, s[46:47]
	s_waitcnt vmcnt(8)
	v_cndmask_b32_e64 v38, 0, v38, s[46:47]
	v_cndmask_b32_e64 v39, 0, v39, s[46:47]
	v_cndmask_b32_e64 v40, 0, v40, s[46:47]
	v_cndmask_b32_e64 v41, 0, v41, s[46:47]
	v_max3_f32 v4, v4, |v22|, |v26|
	v_max3_f32 v5, v5, |v23|, |v27|
	v_max3_f32 v34, v34, |v24|, |v28|
	v_max3_f32 v60, v60, |v25|, |v29|
	v_max3_f32 v62, v4, |v30|, |v38|
	v_max3_f32 v112, v5, |v31|, |v39|
	v_max3_f32 v34, v34, |v32|, |v40|
	v_max3_f32 v113, v60, |v33|, |v41|
	s_lshl_b32 s48, s28, 7
	v_lshl_add_u64 v[4:5], s[48:49], 2, v[2:3]
	s_mul_i32 s48, s28, 0x81
	v_lshl_add_u64 v[60:61], s[48:49], 2, v[2:3]
	s_mul_i32 s48, s28, 0x82
	global_load_dwordx4 v[92:95], v[4:5], off nt
	global_load_dwordx4 v[96:99], v[60:61], off nt
	v_lshl_add_u64 v[4:5], s[48:49], 2, v[2:3]
	s_mul_i32 s48, s28, 0x83
	v_lshl_add_u64 v[60:61], s[48:49], 2, v[2:3]
	s_mul_i32 s48, s28, 0x84
	global_load_dwordx4 v[100:103], v[4:5], off nt
	global_load_dwordx4 v[104:107], v[60:61], off nt
	v_lshl_add_u64 v[4:5], s[48:49], 2, v[2:3]
	s_mul_i32 s48, s28, 0x85
	v_lshl_add_u64 v[60:61], s[48:49], 2, v[2:3]
	s_mul_i32 s48, s28, 0x86
	global_load_dwordx4 v[108:111], v[4:5], off nt
	global_load_dwordx4 v[114:117], v[60:61], off nt
	v_lshl_add_u64 v[4:5], s[48:49], 2, v[2:3]
	s_mul_i32 s48, s28, 0x87
	v_lshl_add_u64 v[60:61], s[48:49], 2, v[2:3]
	global_load_dwordx4 v[120:123], v[4:5], off nt
	global_load_dwordx4 v[124:127], v[60:61], off nt
	s_waitcnt vmcnt(15)
	v_cndmask_b32_e64 v42, 0, v42, s[46:47]
	v_cndmask_b32_e64 v43, 0, v43, s[46:47]
	v_cndmask_b32_e64 v44, 0, v44, s[46:47]
	v_cndmask_b32_e64 v45, 0, v45, s[46:47]
	s_waitcnt vmcnt(14)
	v_cndmask_b32_e64 v63, 0, v64, s[46:47]
	v_cndmask_b32_e64 v64, 0, v65, s[46:47]
	v_cndmask_b32_e64 v65, 0, v66, s[46:47]
	v_cndmask_b32_e64 v66, 0, v67, s[46:47]
	s_waitcnt vmcnt(13)
	v_cndmask_b32_e64 v67, 0, v68, s[46:47]
	v_cndmask_b32_e64 v68, 0, v69, s[46:47]
	v_cndmask_b32_e64 v69, 0, v70, s[46:47]
	v_cndmask_b32_e64 v70, 0, v71, s[46:47]
	s_waitcnt vmcnt(12)
; template <int NCH>
; __device__ __forceinline__ void quant_colblock(const Frame& F, const float* src, int ld_src, int nvalid, unsigned char* dst, int ld_dst, float* sb) {
;     ...
; #pragma unroll
;     for (int bt = 0; bt <= 2 * NCH; ++bt) {
;         if (bt < 2 * NCH) {
; #pragma unroll
;             for (int i = 0; i < 8; ++i) vb[bt & 1][i] = *(const f32x4*)(rb + (size_t)((bt >> 1) * 128 + 8 * (bt & 1) + i) * ld_src + loff); }
;         __builtin_amdgcn_sched_barrier(0);
;         if (bt > 0) { const int pb = bt - 1, c = pb >> 1, hb = pb & 1; f32x4 (&v)[8] = vb[pb & 1]; unsigned t[8][2];
; #pragma unroll
;             for (int i = 0; i < 8; ++i) { v[i].x = ok ? v[i].x : 0.f; v[i].y = ok ? v[i].y : 0.f; v[i].z = ok ? v[i].z : 0.f; v[i].w = ok ? v[i].w : 0.f; }
; #pragma unroll
;             for (int i = 0; i < 8; ++i) { m.x = fmaxf(m.x, fabsf(v[i].x)); m.y = fmaxf(m.y, fabsf(v[i].y)); m.z = fmaxf(m.z, fabsf(v[i].z)); m.w = fmaxf(m.w, fabsf(v[i].w));
	v_cndmask_b32_e64 v71, 0, v72, s[46:47]
	v_cndmask_b32_e64 v72, 0, v73, s[46:47]
	v_cndmask_b32_e64 v73, 0, v74, s[46:47]
	v_cndmask_b32_e64 v74, 0, v75, s[46:47]
	v_max3_f32 v4, v62, |v42|, |v63|
	v_max3_f32 v5, v112, |v43|, |v64|
	v_max3_f32 v34, v34, |v44|, |v65|
	v_max3_f32 v60, v113, |v45|, |v66|
	s_waitcnt vmcnt(11)
	v_cndmask_b32_e64 v75, 0, v76, s[46:47]
	v_cndmask_b32_e64 v76, 0, v77, s[46:47]
	v_cndmask_b32_e64 v77, 0, v78, s[46:47]
	v_cndmask_b32_e64 v78, 0, v79, s[46:47]
	s_waitcnt vmcnt(10)
	v_cndmask_b32_e64 v79, 0, v80, s[46:47]
	v_cndmask_b32_e64 v80, 0, v81, s[46:47]
	v_cndmask_b32_e64 v81, 0, v82, s[46:47]
	v_cndmask_b32_e64 v82, 0, v83, s[46:47]
	v_max3_f32 v4, v4, |v67|, |v71|
	v_max3_f32 v5, v5, |v68|, |v72|
	v_max3_f32 v34, v34, |v69|, |v73|
	v_max3_f32 v60, v60, |v70|, |v74|
	s_waitcnt vmcnt(9)
	v_cndmask_b32_e64 v83, 0, v84, s[46:47]
	v_cndmask_b32_e64 v84, 0, v85, s[46:47]
	v_cndmask_b32_e64 v85, 0, v86, s[46:47]
	v_cndmask_b32_e64 v86, 0, v87, s[46:47]
	s_waitcnt vmcnt(8)
	v_cndmask_b32_e64 v87, 0, v88, s[46:47]
	v_cndmask_b32_e64 v88, 0, v89, s[46:47]
	v_cndmask_b32_e64 v89, 0, v90, s[46:47]
	v_cndmask_b32_e64 v90, 0, v91, s[46:47]
	v_max3_f32 v4, v4, |v75|, |v79|
	v_max3_f32 v5, v5, |v76|, |v80|
	v_max3_f32 v34, v34, |v77|, |v81|
	v_max3_f32 v60, v60, |v78|, |v82|
	v_max3_f32 v62, v4, |v83|, |v87|
	v_max3_f32 v113, v5, |v84|, |v88|
	v_max3_f32 v34, v34, |v85|, |v89|
	v_max3_f32 v136, v60, |v86|, |v90|
	s_mul_i32 s48, s28, 0x88
	v_lshl_add_u64 v[4:5], s[48:49], 2, v[2:3]
	s_mul_i32 s48, s28, 0x89
	v_lshl_add_u64 v[60:61], s[48:49], 2, v[2:3]
	s_mul_i32 s48, s28, 0x8a
	global_load_dwordx4 v[128:131], v[4:5], off nt
	global_load_dwordx4 v[132:135], v[60:61], off nt
	v_lshl_add_u64 v[4:5], s[48:49], 2, v[2:3]
	s_mul_i32 s48, s28, 0x8b
	v_lshl_add_u64 v[60:61], s[48:49], 2, v[2:3]
	s_mul_i32 s48, s28, 0x8c
	global_load_dwordx4 v[140:143], v[4:5], off nt
	global_load_dwordx4 v[144:147], v[60:61], off nt
	v_lshl_add_u64 v[4:5], s[48:49], 2, v[2:3]
	s_mul_i32 s48, s28, 0x8d
	v_lshl_add_u64 v[60:61], s[48:49], 2, v[2:3]
	s_mul_i32 s48, s28, 0x8e
	global_load_dwordx4 v[148:151], v[4:5], off nt
	global_load_dwordx4 v[152:155], v[60:61], off nt
	v_lshl_add_u64 v[4:5], s[48:49], 2, v[2:3]
	s_mul_i32 s48, s28, 0x8f
	v_lshl_add_u64 v[60:61], s[48:49], 2, v[2:3]
	global_load_dwordx4 v[156:159], v[4:5], off nt
	global_load_dwordx4 v[160:163], v[60:61], off nt
	s_waitcnt vmcnt(15)
	v_cndmask_b32_e64 v91, 0, v92, s[46:47]
	v_cndmask_b32_e64 v92, 0, v93, s[46:47]
	v_cndmask_b32_e64 v93, 0, v94, s[46:47]
	v_cndmask_b32_e64 v94, 0, v95, s[46:47]
	s_waitcnt vmcnt(14)
	v_cndmask_b32_e64 v95, 0, v96, s[46:47]
	v_cndmask_b32_e64 v96, 0, v97, s[46:47]
	v_cndmask_b32_e64 v97, 0, v98, s[46:47]
	v_cndmask_b32_e64 v98, 0, v99, s[46:47]
	s_waitcnt vmcnt(13)
	v_cndmask_b32_e64 v99, 0, v100, s[46:47]
	v_cndmask_b32_e64 v100, 0, v101, s[46:47]
	v_cndmask_b32_e64 v101, 0, v102, s[46:47]
	v_cndmask_b32_e64 v102, 0, v103, s[46:47]
	s_waitcnt vmcnt(12)
	v_cndmask_b32_e64 v103, 0, v104, s[46:47]
	v_cndmask_b32_e64 v104, 0, v105, s[46:47]
	v_cndmask_b32_e64 v105, 0, v106, s[46:47]
	v_max3_f32 v4, v62, |v91|, |v95|
	v_max3_f32 v34, v34, |v93|, |v97|
	v_cndmask_b32_e64 v106, 0, v107, s[46:47]
	s_waitcnt vmcnt(11)
	v_cndmask_b32_e64 v107, 0, v108, s[46:47]
	v_cndmask_b32_e64 v110, 0, v110, s[46:47]
	s_waitcnt vmcnt(10)
	v_cndmask_b32_e64 v112, 0, v114, s[46:47]
	v_cndmask_b32_e64 v114, 0, v115, s[46:47]
	v_cndmask_b32_e64 v115, 0, v116, s[46:47]
	v_max3_f32 v5, v113, |v92|, |v96|
	v_max3_f32 v60, v136, |v94|, |v98|
	v_max3_f32 v4, v4, |v99|, |v103|
	v_max3_f32 v34, v34, |v101|, |v105|
	v_cndmask_b32_e64 v108, 0, v109, s[46:47]
	v_cndmask_b32_e64 v111, 0, v111, s[46:47]
	v_cndmask_b32_e64 v116, 0, v117, s[46:47]
	s_waitcnt vmcnt(9)
	v_cndmask_b32_e64 v118, 0, v120, s[46:47]
	v_cndmask_b32_e64 v119, 0, v121, s[46:47]
	v_cndmask_b32_e64 v121, 0, v122, s[46:47]
	v_cndmask_b32_e64 v122, 0, v123, s[46:47]
	s_waitcnt vmcnt(8)
	v_cndmask_b32_e64 v123, 0, v124, s[46:47]
	v_cndmask_b32_e64 v124, 0, v125, s[46:47]
	v_cndmask_b32_e64 v125, 0, v126, s[46:47]
	v_max3_f32 v5, v5, |v100|, |v104|
	v_max3_f32 v60, v60, |v102|, |v106|
	v_max3_f32 v4, v4, |v107|, |v112|
	v_max3_f32 v34, v34, |v110|, |v115|
	v_cndmask_b32_e64 v126, 0, v127, s[46:47]
	v_max3_f32 v5, v5, |v108|, |v114|
	v_max3_f32 v60, v60, |v111|, |v116|
	v_max3_f32 v62, v4, |v118|, |v123|
	v_max3_f32 v34, v34, |v121|, |v125|
	v_max3_f32 v192, v5, |v119|, |v124|
	v_max3_f32 v193, v60, |v122|, |v126|
	s_lshl_b32 s48, s28, 8
	v_lshl_add_u64 v[4:5], s[48:49], 2, v[2:3]
	s_mul_i32 s48, s28, 0x101
	v_lshl_add_u64 v[60:61], s[48:49], 2, v[2:3]
	s_mul_i32 s48, s28, 0x102
	global_load_dwordx4 v[164:167], v[4:5], off nt
	global_load_dwordx4 v[168:171], v[60:61], off nt
	v_lshl_add_u64 v[4:5], s[48:49], 2, v[2:3]
	s_mul_i32 s48, s28, 0x103
	v_lshl_add_u64 v[60:61], s[48:49], 2, v[2:3]
	s_mul_i32 s48, s28, 0x104
	global_load_dwordx4 v[172:175], v[4:5], off nt
	global_load_dwordx4 v[176:179], v[60:61], off nt
	v_lshl_add_u64 v[4:5], s[48:49], 2, v[2:3]
	s_mul_i32 s48, s28, 0x105
	v_lshl_add_u64 v[60:61], s[48:49], 2, v[2:3]
	s_mul_i32 s48, s28, 0x106
	global_load_dwordx4 v[180:183], v[4:5], off nt
	global_load_dwordx4 v[184:187], v[60:61], off nt
	v_lshl_add_u64 v[4:5], s[48:49], 2, v[2:3]
	s_mul_i32 s48, s28, 0x107
	v_lshl_add_u64 v[60:61], s[48:49], 2, v[2:3]
	global_load_dwordx4 v[188:191], v[4:5], off nt
	global_load_dwordx4 v[196:199], v[60:61], off nt
	s_waitcnt vmcnt(15)
	v_cndmask_b32_e64 v127, 0, v128, s[46:47]
	v_cndmask_b32_e64 v120, 0, v130, s[46:47]
	s_waitcnt vmcnt(14)
; template <int NCH>
; __device__ __forceinline__ void quant_colblock(const Frame& F, const float* src, int ld_src, int nvalid, unsigned char* dst, int ld_dst, float* sb) {
;     ...
; #pragma unroll
;     for (int bt = 0; bt <= 2 * NCH; ++bt) {
;         if (bt < 2 * NCH) {
; #pragma unroll
;             for (int i = 0; i < 8; ++i) vb[bt & 1][i] = *(const f32x4*)(rb + (size_t)((bt >> 1) * 128 + 8 * (bt & 1) + i) * ld_src + loff); }
;         __builtin_amdgcn_sched_barrier(0);
;         if (bt > 0) { const int pb = bt - 1, c = pb >> 1, hb = pb & 1; f32x4 (&v)[8] = vb[pb & 1]; unsigned t[8][2];
; #pragma unroll
;             for (int i = 0; i < 8; ++i) { v[i].x = ok ? v[i].x : 0.f; v[i].y = ok ? v[i].y : 0.f; v[i].z = ok ? v[i].z : 0.f; v[i].w = ok ? v[i].w : 0.f; }
; #pragma unroll
;             for (int i = 0; i < 8; ++i) { m.x = fmaxf(m.x, fabsf(v[i].x)); m.y = fmaxf(m.y, fabsf(v[i].y)); m.z = fmaxf(m.z, fabsf(v[i].z)); m.w = fmaxf(m.w, fabsf(v[i].w));
	v_cndmask_b32_e64 v130, 0, v132, s[46:47]
	v_cndmask_b32_e64 v117, 0, v134, s[46:47]
	v_cndmask_b32_e64 v128, 0, v129, s[46:47]
	v_cndmask_b32_e64 v129, 0, v131, s[46:47]
	v_cndmask_b32_e64 v131, 0, v133, s[46:47]
	v_cndmask_b32_e64 v132, 0, v135, s[46:47]
	s_waitcnt vmcnt(13)
	v_cndmask_b32_e64 v133, 0, v140, s[46:47]
	v_cndmask_b32_e64 v113, 0, v142, s[46:47]
	s_waitcnt vmcnt(12)
	v_cndmask_b32_e64 v136, 0, v144, s[46:47]
	v_cndmask_b32_e64 v109, 0, v146, s[46:47]
	v_max3_f32 v4, v62, |v127|, |v130|
	v_max3_f32 v34, v34, |v120|, |v117|
	v_cndmask_b32_e64 v134, 0, v141, s[46:47]
	v_cndmask_b32_e64 v135, 0, v143, s[46:47]
	v_cndmask_b32_e64 v137, 0, v145, s[46:47]
	v_cndmask_b32_e64 v140, 0, v147, s[46:47]
	s_waitcnt vmcnt(11)
	v_cndmask_b32_e64 v141, 0, v148, s[46:47]
	v_cndmask_b32_e64 v143, 0, v150, s[46:47]
	s_waitcnt vmcnt(10)
	v_cndmask_b32_e64 v145, 0, v152, s[46:47]
	v_cndmask_b32_e64 v147, 0, v154, s[46:47]
	v_max3_f32 v5, v192, |v128|, |v131|
	v_max3_f32 v60, v193, |v129|, |v132|
	v_max3_f32 v4, v4, |v133|, |v136|
	v_max3_f32 v34, v34, |v113|, |v109|
	v_cndmask_b32_e64 v142, 0, v149, s[46:47]
	v_cndmask_b32_e64 v144, 0, v151, s[46:47]
	v_cndmask_b32_e64 v146, 0, v153, s[46:47]
	v_cndmask_b32_e64 v148, 0, v155, s[46:47]
	s_waitcnt vmcnt(9)
	v_cndmask_b32_e64 v149, 0, v156, s[46:47]
	v_cndmask_b32_e64 v151, 0, v158, s[46:47]
	s_waitcnt vmcnt(8)
	v_cndmask_b32_e64 v153, 0, v160, s[46:47]
	v_cndmask_b32_e64 v155, 0, v162, s[46:47]
	v_max3_f32 v5, v5, |v134|, |v137|
	v_max3_f32 v60, v60, |v135|, |v140|
	v_max3_f32 v4, v4, |v141|, |v145|
	v_max3_f32 v34, v34, |v143|, |v147|
	v_cndmask_b32_e64 v150, 0, v157, s[46:47]
	v_cndmask_b32_e64 v152, 0, v159, s[46:47]
	v_cndmask_b32_e64 v154, 0, v161, s[46:47]
	v_cndmask_b32_e64 v156, 0, v163, s[46:47]
	v_max3_f32 v5, v5, |v142|, |v146|
	v_max3_f32 v60, v60, |v144|, |v148|
	v_max3_f32 v62, v4, |v149|, |v153|
	v_max3_f32 v34, v34, |v151|, |v155|
	v_max3_f32 v157, v5, |v150|, |v154|
	v_max3_f32 v162, v60, |v152|, |v156|
	s_mul_i32 s48, s28, 0x108
	v_lshl_add_u64 v[4:5], s[48:49], 2, v[2:3]
	s_mul_i32 s48, s28, 0x109
	v_lshl_add_u64 v[60:61], s[48:49], 2, v[2:3]
	s_mul_i32 s48, s28, 0x10a
	global_load_dwordx4 v[158:161], v[4:5], off nt
	global_load_dwordx4 v[200:203], v[60:61], off nt
	v_lshl_add_u64 v[4:5], s[48:49], 2, v[2:3]
	s_mul_i32 s48, s28, 0x10b
	v_lshl_add_u64 v[60:61], s[48:49], 2, v[2:3]
	s_mul_i32 s48, s28, 0x10c
	global_load_dwordx4 v[204:207], v[4:5], off nt
	global_load_dwordx4 v[208:211], v[60:61], off nt
	v_lshl_add_u64 v[4:5], s[48:49], 2, v[2:3]
	s_mul_i32 s48, s28, 0x10d
	v_lshl_add_u64 v[60:61], s[48:49], 2, v[2:3]
	s_mul_i32 s48, s28, 0x10e
	global_load_dwordx4 v[212:215], v[4:5], off nt
	global_load_dwordx4 v[216:219], v[60:61], off nt
	v_lshl_add_u64 v[4:5], s[48:49], 2, v[2:3]
	s_mul_i32 s48, s28, 0x10f
	v_lshl_add_u64 v[60:61], s[48:49], 2, v[2:3]
	global_load_dwordx4 v[220:223], v[4:5], off nt
	global_load_dwordx4 v[224:227], v[60:61], off nt
	s_waitcnt vmcnt(15)
	v_cndmask_b32_e64 v4, 0, v164, s[46:47]
	v_cndmask_b32_e64 v60, 0, v166, s[46:47]
	s_waitcnt vmcnt(14)
	v_cndmask_b32_e64 v192, 0, v168, s[46:47]
	v_cndmask_b32_e64 v195, 0, v170, s[46:47]
	v_cndmask_b32_e64 v5, 0, v165, s[46:47]
	v_cndmask_b32_e64 v61, 0, v167, s[46:47]
	v_cndmask_b32_e64 v193, 0, v169, s[46:47]
	v_cndmask_b32_e64 v228, 0, v171, s[46:47]
	s_waitcnt vmcnt(13)
	v_cndmask_b32_e64 v170, 0, v172, s[46:47]
	v_cndmask_b32_e64 v229, 0, v173, s[46:47]
	v_cndmask_b32_e64 v171, 0, v174, s[46:47]
	s_waitcnt vmcnt(12)
	v_cndmask_b32_e64 v172, 0, v176, s[46:47]
	v_cndmask_b32_e64 v173, 0, v178, s[46:47]
	v_max3_f32 v62, v62, |v4|, |v192|
	v_max3_f32 v34, v34, |v60|, |v195|
	v_cndmask_b32_e64 v174, 0, v175, s[46:47]
	v_cndmask_b32_e64 v175, 0, v177, s[46:47]
	v_cndmask_b32_e64 v176, 0, v179, s[46:47]
	s_waitcnt vmcnt(11)
	v_cndmask_b32_e64 v166, 0, v180, s[46:47]
	v_cndmask_b32_e64 v167, 0, v182, s[46:47]
	s_waitcnt vmcnt(10)
	v_cndmask_b32_e64 v168, 0, v184, s[46:47]
	v_cndmask_b32_e64 v169, 0, v186, s[46:47]
	v_max3_f32 v157, v157, |v5|, |v193|
	v_max3_f32 v162, v162, |v61|, |v228|
	v_max3_f32 v62, v62, |v170|, |v172|
	v_max3_f32 v34, v34, |v171|, |v173|
	v_cndmask_b32_e64 v177, 0, v181, s[46:47]
	v_cndmask_b32_e64 v178, 0, v183, s[46:47]
	v_cndmask_b32_e64 v179, 0, v185, s[46:47]
	v_cndmask_b32_e64 v180, 0, v187, s[46:47]
	s_waitcnt vmcnt(9)
	v_cndmask_b32_e64 v181, 0, v188, s[46:47]
	v_cndmask_b32_e64 v163, 0, v190, s[46:47]
	s_waitcnt vmcnt(8)
; template <int NCH>
; __device__ __forceinline__ void quant_colblock(const Frame& F, const float* src, int ld_src, int nvalid, unsigned char* dst, int ld_dst, float* sb) {
;     ...
;     for (int bt = 0; bt <= 2 * NCH; ++bt) {
;         if (bt < 2 * NCH) {
; #pragma unroll
;             for (int i = 0; i < 8; ++i) vb[bt & 1][i] = *(const f32x4*)(rb + (size_t)((bt >> 1) * 128 + 8 * (bt & 1) + i) * ld_src + loff); }
;         __builtin_amdgcn_sched_barrier(0);
;         if (bt > 0) { const int pb = bt - 1, c = pb >> 1, hb = pb & 1; f32x4 (&v)[8] = vb[pb & 1]; unsigned t[8][2];
; #pragma unroll
;             for (int i = 0; i < 8; ++i) { v[i].x = ok ? v[i].x : 0.f; v[i].y = ok ? v[i].y : 0.f; v[i].z = ok ? v[i].z : 0.f; v[i].w = ok ? v[i].w : 0.f; }
; #pragma unroll
;             for (int i = 0; i < 8; ++i) { m.x = fmaxf(m.x, fabsf(v[i].x)); m.y = fmaxf(m.y, fabsf(v[i].y)); m.z = fmaxf(m.z, fabsf(v[i].z)); m.w = fmaxf(m.w, fabsf(v[i].w));
;                 t[i][0] = __builtin_bit_cast(unsigned, __builtin_amdgcn_cvt_pkrtz(v[i].x, v[i].y)); t[i][1] = __builtin_bit_cast(unsigned, __builtin_amdgcn_cvt_pkrtz(v[i].z, v[i].w)); }
;             if (c < NREG) {
; #pragma unroll
;                 for (int i = 0; i < 8; ++i) { h[c < NREG ? c : 0][8 * hb + i][0] = t[i][0]; h[c < NREG ? c : 0][8 * hb + i][1] = t[i][1]; } }
;             else {
; #pragma unroll
;                 for (int e = 0; e < 4; ++e) hl[((c - 2) * 8 + 4 * hb + e) * 512] = (u32x4){t[2 * e][0], t[2 * e][1], t[2 * e + 1][0], t[2 * e + 1][1]}; }
;             __builtin_amdgcn_sched_barrier(0); } }
	v_cndmask_b32_e64 v164, 0, v196, s[46:47]
	v_cndmask_b32_e64 v165, 0, v198, s[46:47]
	v_max3_f32 v157, v157, |v229|, |v175|
	v_max3_f32 v162, v162, |v174|, |v176|
	v_max3_f32 v62, v62, |v166|, |v168|
	v_max3_f32 v34, v34, |v167|, |v169|
	v_cndmask_b32_e64 v182, 0, v189, s[46:47]
	v_cndmask_b32_e64 v183, 0, v191, s[46:47]
	v_cndmask_b32_e64 v184, 0, v197, s[46:47]
	v_cndmask_b32_e64 v185, 0, v199, s[46:47]
	v_max3_f32 v157, v157, |v177|, |v179|
	v_max3_f32 v162, v162, |v178|, |v180|
	v_max3_f32 v62, v62, |v181|, |v164|
	v_max3_f32 v34, v34, |v163|, |v165|
	v_cvt_pkrtz_f16_f32 v166, v166, v177
	v_cvt_pkrtz_f16_f32 v173, v173, v176
	v_cvt_pkrtz_f16_f32 v172, v172, v175
	v_cvt_pkrtz_f16_f32 v171, v171, v174
	v_cvt_pkrtz_f16_f32 v177, v195, v228
	v_cvt_pkrtz_f16_f32 v176, v192, v193
	v_cvt_pkrtz_f16_f32 v175, v60, v61
	v_cvt_pkrtz_f16_f32 v174, v4, v5
	v_max3_f32 v157, v157, |v182|, |v184|
	v_max3_f32 v196, v162, |v183|, |v185|
	v_cvt_pkrtz_f16_f32 v165, v165, v185
	v_cvt_pkrtz_f16_f32 v164, v164, v184
	v_cvt_pkrtz_f16_f32 v163, v163, v183
	v_cvt_pkrtz_f16_f32 v162, v181, v182
	v_cvt_pkrtz_f16_f32 v169, v169, v180
	v_cvt_pkrtz_f16_f32 v168, v168, v179
	v_cvt_pkrtz_f16_f32 v167, v167, v178
	v_cvt_pkrtz_f16_f32 v170, v170, v229
	ds_write_b128 v46, v[174:177] offset:4096
	ds_write_b128 v46, v[170:173] offset:12288
	ds_write_b128 v46, v[166:169] offset:20480
	ds_write_b128 v46, v[162:165] offset:28672
	s_mul_i32 s48, s28, 0x180
	v_lshl_add_u64 v[4:5], s[48:49], 2, v[2:3]
	s_mul_i32 s48, s28, 0x181
	v_lshl_add_u64 v[60:61], s[48:49], 2, v[2:3]
	s_mul_i32 s48, s28, 0x182
	global_load_dwordx4 v[162:165], v[4:5], off nt
	global_load_dwordx4 v[166:169], v[60:61], off nt
	v_lshl_add_u64 v[4:5], s[48:49], 2, v[2:3]
	s_mul_i32 s48, s28, 0x183
	v_lshl_add_u64 v[60:61], s[48:49], 2, v[2:3]
	s_mul_i32 s48, s28, 0x184
	global_load_dwordx4 v[170:173], v[4:5], off nt
	global_load_dwordx4 v[174:177], v[60:61], off nt
	v_lshl_add_u64 v[4:5], s[48:49], 2, v[2:3]
	s_mul_i32 s48, s28, 0x185
	v_lshl_add_u64 v[60:61], s[48:49], 2, v[2:3]
	s_mul_i32 s48, s28, 0x186
	global_load_dwordx4 v[178:181], v[4:5], off nt
	global_load_dwordx4 v[182:185], v[60:61], off nt
	v_lshl_add_u64 v[4:5], s[48:49], 2, v[2:3]
	s_mul_i32 s48, s28, 0x187
	v_lshl_add_u64 v[60:61], s[48:49], 2, v[2:3]
	global_load_dwordx4 v[186:189], v[4:5], off nt
	global_load_dwordx4 v[190:193], v[60:61], off nt
	s_waitcnt vmcnt(15)
	v_cndmask_b32_e64 v4, 0, v158, s[46:47]
	v_cndmask_b32_e64 v60, 0, v160, s[46:47]
	s_waitcnt vmcnt(14)
	v_cndmask_b32_e64 v195, 0, v200, s[46:47]
	v_cndmask_b32_e64 v229, 0, v202, s[46:47]
	v_cndmask_b32_e64 v5, 0, v159, s[46:47]
	v_cndmask_b32_e64 v61, 0, v161, s[46:47]
	v_cndmask_b32_e64 v228, 0, v201, s[46:47]
	v_cndmask_b32_e64 v230, 0, v203, s[46:47]
	s_waitcnt vmcnt(13)
	v_cndmask_b32_e64 v200, 0, v204, s[46:47]
	v_cndmask_b32_e64 v201, 0, v206, s[46:47]
	s_waitcnt vmcnt(12)
	v_cndmask_b32_e64 v202, 0, v208, s[46:47]
	v_cndmask_b32_e64 v203, 0, v210, s[46:47]
	v_max3_f32 v62, v62, |v4|, |v195|
	v_max3_f32 v34, v34, |v60|, |v229|
	v_cndmask_b32_e64 v204, 0, v205, s[46:47]
	v_cndmask_b32_e64 v205, 0, v207, s[46:47]
	v_cndmask_b32_e64 v206, 0, v209, s[46:47]
	v_cndmask_b32_e64 v207, 0, v211, s[46:47]
	s_waitcnt vmcnt(11)
	v_cndmask_b32_e64 v208, 0, v212, s[46:47]
	v_cndmask_b32_e64 v197, 0, v214, s[46:47]
	s_waitcnt vmcnt(10)
	v_cndmask_b32_e64 v198, 0, v216, s[46:47]
	v_cndmask_b32_e64 v199, 0, v218, s[46:47]
	v_max3_f32 v157, v157, |v5|, |v228|
	v_max3_f32 v196, v196, |v61|, |v230|
	v_max3_f32 v62, v62, |v200|, |v202|
	v_max3_f32 v34, v34, |v201|, |v203|
	v_cndmask_b32_e64 v209, 0, v213, s[46:47]
	v_cndmask_b32_e64 v210, 0, v215, s[46:47]
	v_cndmask_b32_e64 v211, 0, v217, s[46:47]
	v_cndmask_b32_e64 v212, 0, v219, s[46:47]
	s_waitcnt vmcnt(9)
	v_cndmask_b32_e64 v158, 0, v220, s[46:47]
	v_cndmask_b32_e64 v159, 0, v222, s[46:47]
	s_waitcnt vmcnt(8)
	v_cndmask_b32_e64 v160, 0, v224, s[46:47]
	v_cndmask_b32_e64 v161, 0, v226, s[46:47]
	v_max3_f32 v157, v157, |v204|, |v206|
	v_max3_f32 v196, v196, |v205|, |v207|
	v_max3_f32 v62, v62, |v208|, |v198|
	v_max3_f32 v34, v34, |v197|, |v199|
	v_cndmask_b32_e64 v213, 0, v221, s[46:47]
	v_cndmask_b32_e64 v214, 0, v223, s[46:47]
	v_cndmask_b32_e64 v215, 0, v225, s[46:47]
	v_cndmask_b32_e64 v216, 0, v227, s[46:47]
	v_max3_f32 v157, v157, |v209|, |v211|
	v_max3_f32 v196, v196, |v210|, |v212|
	v_max3_f32 v62, v62, |v158|, |v160|
	v_max3_f32 v34, v34, |v159|, |v161|
	v_cvt_pkrtz_f16_f32 v203, v203, v207
	v_cvt_pkrtz_f16_f32 v202, v202, v206
	v_cvt_pkrtz_f16_f32 v201, v201, v205
	v_cvt_pkrtz_f16_f32 v200, v200, v204
	v_cvt_pkrtz_f16_f32 v207, v229, v230
	v_cvt_pkrtz_f16_f32 v206, v195, v228
	v_cvt_pkrtz_f16_f32 v205, v60, v61
	v_cvt_pkrtz_f16_f32 v204, v4, v5
	v_max3_f32 v157, v157, |v213|, |v215|
	v_max3_f32 v220, v196, |v214|, |v216|
	v_cvt_pkrtz_f16_f32 v161, v161, v216
	v_cvt_pkrtz_f16_f32 v160, v160, v215
	v_cvt_pkrtz_f16_f32 v159, v159, v214
	v_cvt_pkrtz_f16_f32 v158, v158, v213
	v_cvt_pkrtz_f16_f32 v199, v199, v212
	v_cvt_pkrtz_f16_f32 v198, v198, v211
	v_cvt_pkrtz_f16_f32 v197, v197, v210
	v_cvt_pkrtz_f16_f32 v196, v208, v209
	ds_write_b128 v46, v[204:207] offset:36864
	ds_write_b128 v46, v[200:203] offset:45056
	ds_write_b128 v46, v[196:199] offset:53248
	ds_write_b128 v46, v[158:161] offset:61440
	s_mul_i32 s48, s28, 0x188
	v_lshl_add_u64 v[4:5], s[48:49], 2, v[2:3]
	s_mul_i32 s48, s28, 0x189
	v_lshl_add_u64 v[60:61], s[48:49], 2, v[2:3]
	s_mul_i32 s48, s28, 0x18a
	global_load_dwordx4 v[158:161], v[4:5], off nt
	global_load_dwordx4 v[196:199], v[60:61], off nt
	v_lshl_add_u64 v[4:5], s[48:49], 2, v[2:3]
	s_mul_i32 s48, s28, 0x18b
	v_lshl_add_u64 v[60:61], s[48:49], 2, v[2:3]
	s_mul_i32 s48, s28, 0x18c
	global_load_dwordx4 v[200:203], v[4:5], off nt
	global_load_dwordx4 v[204:207], v[60:61], off nt
	v_lshl_add_u64 v[4:5], s[48:49], 2, v[2:3]
	s_mul_i32 s48, s28, 0x18d
	v_lshl_add_u64 v[60:61], s[48:49], 2, v[2:3]
	s_mul_i32 s48, s28, 0x18e
	global_load_dwordx4 v[208:211], v[4:5], off nt
	global_load_dwordx4 v[212:215], v[60:61], off nt
	v_lshl_add_u64 v[4:5], s[48:49], 2, v[2:3]
	s_mulk_i32 s28, 0x18f
	v_lshl_add_u64 v[60:61], s[28:29], 2, v[2:3]
	global_load_dwordx4 v[2:5], v[4:5], off nt
	s_nop 0
	global_load_dwordx4 v[216:219], v[60:61], off nt
	s_waitcnt vmcnt(15)
; #define LAS __attribute__((address_space(3)))
; template <int NCH>
; __device__ __forceinline__ void quant_colblock(const Frame& F, const float* src, int ld_src, int nvalid, unsigned char* dst, int ld_dst, float* sb) {
;     ...
;             for (int i = 0; i < 8; ++i) vb[bt & 1][i] = *(const f32x4*)(rb + (size_t)((bt >> 1) * 128 + 8 * (bt & 1) + i) * ld_src + loff); }
;         __builtin_amdgcn_sched_barrier(0);
;         if (bt > 0) { const int pb = bt - 1, c = pb >> 1, hb = pb & 1; f32x4 (&v)[8] = vb[pb & 1]; unsigned t[8][2];
; #pragma unroll
;             for (int i = 0; i < 8; ++i) { v[i].x = ok ? v[i].x : 0.f; v[i].y = ok ? v[i].y : 0.f; v[i].z = ok ? v[i].z : 0.f; v[i].w = ok ? v[i].w : 0.f; }
; #pragma unroll
;             for (int i = 0; i < 8; ++i) { m.x = fmaxf(m.x, fabsf(v[i].x)); m.y = fmaxf(m.y, fabsf(v[i].y)); m.z = fmaxf(m.z, fabsf(v[i].z)); m.w = fmaxf(m.w, fabsf(v[i].w));
;                 t[i][0] = __builtin_bit_cast(unsigned, __builtin_amdgcn_cvt_pkrtz(v[i].x, v[i].y)); t[i][1] = __builtin_bit_cast(unsigned, __builtin_amdgcn_cvt_pkrtz(v[i].z, v[i].w)); }
;             if (c < NREG) {
; #pragma unroll
;                 for (int i = 0; i < 8; ++i) { h[c < NREG ? c : 0][8 * hb + i][0] = t[i][0]; h[c < NREG ? c : 0][8 * hb + i][1] = t[i][1]; } }
;             else {
; #pragma unroll
;                 for (int e = 0; e < 4; ++e) hl[((c - 2) * 8 + 4 * hb + e) * 512] = (u32x4){t[2 * e][0], t[2 * e][1], t[2 * e + 1][0], t[2 * e + 1][1]}; }
;             __builtin_amdgcn_sched_barrier(0); } }
; #pragma unroll
;     for (int sh = 8; sh < 64; sh <<= 1) { m.x = fmaxf(m.x, __shfl_xor(m.x, sh)); m.y = fmaxf(m.y, __shfl_xor(m.y, sh)); m.z = fmaxf(m.z, __shfl_xor(m.z, sh)); m.w = fmaxf(m.w, __shfl_xor(m.w, sh)); }
;     if (kg == 0) *(LAS f32x4*)(cm + w * 32 + n) = m;
	v_cndmask_b32_e64 v60, 0, v162, s[46:47]
	v_cndmask_b32_e64 v195, 0, v164, s[46:47]
	s_waitcnt vmcnt(14)
	v_cndmask_b32_e64 v222, 0, v166, s[46:47]
	v_cndmask_b32_e64 v224, 0, v168, s[46:47]
	v_cndmask_b32_e64 v61, 0, v163, s[46:47]
	v_cndmask_b32_e64 v221, 0, v165, s[46:47]
	v_cndmask_b32_e64 v223, 0, v167, s[46:47]
	v_cndmask_b32_e64 v225, 0, v169, s[46:47]
	s_waitcnt vmcnt(13)
	v_cndmask_b32_e64 v170, 0, v170, s[46:47]
	v_cndmask_b32_e64 v226, 0, v171, s[46:47]
	v_cndmask_b32_e64 v171, 0, v172, s[46:47]
	v_cndmask_b32_e64 v227, 0, v173, s[46:47]
	s_waitcnt vmcnt(12)
	v_cndmask_b32_e64 v172, 0, v174, s[46:47]
	v_cndmask_b32_e64 v173, 0, v176, s[46:47]
	v_max3_f32 v62, v62, |v60|, |v222|
	v_max3_f32 v34, v34, |v195|, |v224|
	v_cndmask_b32_e64 v174, 0, v175, s[46:47]
	v_cndmask_b32_e64 v175, 0, v177, s[46:47]
	s_waitcnt vmcnt(11)
	v_cndmask_b32_e64 v166, 0, v178, s[46:47]
	v_cndmask_b32_e64 v167, 0, v180, s[46:47]
	s_waitcnt vmcnt(10)
	v_cndmask_b32_e64 v168, 0, v182, s[46:47]
	v_cndmask_b32_e64 v169, 0, v184, s[46:47]
	v_max3_f32 v157, v157, |v61|, |v223|
	v_max3_f32 v184, v220, |v221|, |v225|
	v_max3_f32 v62, v62, |v170|, |v172|
	v_max3_f32 v34, v34, |v171|, |v173|
	v_cndmask_b32_e64 v176, 0, v179, s[46:47]
	v_cndmask_b32_e64 v177, 0, v181, s[46:47]
	v_cndmask_b32_e64 v178, 0, v183, s[46:47]
	v_cndmask_b32_e64 v179, 0, v185, s[46:47]
	s_waitcnt vmcnt(9)
	v_cndmask_b32_e64 v162, 0, v186, s[46:47]
	v_cndmask_b32_e64 v163, 0, v188, s[46:47]
	s_waitcnt vmcnt(8)
	v_cndmask_b32_e64 v164, 0, v190, s[46:47]
	v_cndmask_b32_e64 v165, 0, v192, s[46:47]
	v_max3_f32 v157, v157, |v226|, |v174|
	v_max3_f32 v184, v184, |v227|, |v175|
	v_max3_f32 v62, v62, |v166|, |v168|
	v_max3_f32 v34, v34, |v167|, |v169|
	v_cndmask_b32_e64 v180, 0, v187, s[46:47]
	v_cndmask_b32_e64 v181, 0, v189, s[46:47]
	v_cndmask_b32_e64 v182, 0, v191, s[46:47]
	v_cndmask_b32_e64 v183, 0, v193, s[46:47]
	v_max3_f32 v157, v157, |v176|, |v178|
	v_max3_f32 v184, v184, |v177|, |v179|
	v_max3_f32 v62, v62, |v162|, |v164|
	v_max3_f32 v34, v34, |v163|, |v165|
	v_cvt_pkrtz_f16_f32 v167, v167, v177
	v_cvt_pkrtz_f16_f32 v166, v166, v176
	v_cvt_pkrtz_f16_f32 v173, v173, v175
	v_cvt_pkrtz_f16_f32 v172, v172, v174
	v_cvt_pkrtz_f16_f32 v177, v224, v225
	v_cvt_pkrtz_f16_f32 v176, v222, v223
	v_cvt_pkrtz_f16_f32 v175, v195, v221
	v_cvt_pkrtz_f16_f32 v174, v60, v61
	v_max3_f32 v157, v157, |v180|, |v182|
	v_max3_f32 v184, v184, |v181|, |v183|
	v_cvt_pkrtz_f16_f32 v165, v165, v183
	v_cvt_pkrtz_f16_f32 v164, v164, v182
	v_cvt_pkrtz_f16_f32 v163, v163, v181
	v_cvt_pkrtz_f16_f32 v162, v162, v180
	v_cvt_pkrtz_f16_f32 v169, v169, v179
	v_cvt_pkrtz_f16_f32 v168, v168, v178
	v_cvt_pkrtz_f16_f32 v171, v171, v227
	v_cvt_pkrtz_f16_f32 v170, v170, v226
	ds_write_b128 v48, v[174:177]
	ds_write_b128 v49, v[170:173]
	ds_write_b128 v50, v[166:169]
	ds_write_b128 v51, v[162:165]
	s_waitcnt vmcnt(7)
	v_cndmask_b32_e64 v60, 0, v158, s[46:47]
	v_cndmask_b32_e64 v166, 0, v160, s[46:47]
	s_waitcnt vmcnt(6)
	v_cndmask_b32_e64 v168, 0, v196, s[46:47]
	v_cndmask_b32_e64 v169, 0, v198, s[46:47]
	v_cndmask_b32_e64 v61, 0, v159, s[46:47]
	v_cndmask_b32_e64 v167, 0, v161, s[46:47]
	v_cndmask_b32_e64 v170, 0, v197, s[46:47]
	v_cndmask_b32_e64 v171, 0, v199, s[46:47]
	s_waitcnt vmcnt(5)
	v_cndmask_b32_e64 v162, 0, v200, s[46:47]
	v_cndmask_b32_e64 v163, 0, v202, s[46:47]
	s_waitcnt vmcnt(4)
	v_cndmask_b32_e64 v164, 0, v204, s[46:47]
	v_cndmask_b32_e64 v165, 0, v206, s[46:47]
	v_max3_f32 v62, v62, |v60|, |v168|
	v_max3_f32 v34, v34, |v166|, |v169|
	v_cndmask_b32_e64 v172, 0, v201, s[46:47]
	v_cndmask_b32_e64 v173, 0, v203, s[46:47]
	v_cndmask_b32_e64 v174, 0, v205, s[46:47]
	v_cndmask_b32_e64 v175, 0, v207, s[46:47]
	s_waitcnt vmcnt(3)
	v_cndmask_b32_e64 v158, 0, v208, s[46:47]
	v_cndmask_b32_e64 v159, 0, v210, s[46:47]
	s_waitcnt vmcnt(2)
	v_cndmask_b32_e64 v160, 0, v212, s[46:47]
	v_cndmask_b32_e64 v161, 0, v214, s[46:47]
	v_max3_f32 v157, v157, |v61|, |v170|
	v_max3_f32 v184, v184, |v167|, |v171|
	v_max3_f32 v62, v62, |v162|, |v164|
	v_max3_f32 v34, v34, |v163|, |v165|
	v_cndmask_b32_e64 v176, 0, v209, s[46:47]
	v_cndmask_b32_e64 v177, 0, v211, s[46:47]
	v_cndmask_b32_e64 v178, 0, v213, s[46:47]
	v_cndmask_b32_e64 v179, 0, v215, s[46:47]
	s_waitcnt vmcnt(1)
	v_cndmask_b32_e64 v2, 0, v2, s[46:47]
	v_cndmask_b32_e64 v180, 0, v3, s[46:47]
	v_cndmask_b32_e64 v3, 0, v4, s[46:47]
	v_cndmask_b32_e64 v181, 0, v5, s[46:47]
	s_waitcnt vmcnt(0)
	v_cndmask_b32_e64 v4, 0, v216, s[46:47]
	v_cndmask_b32_e64 v182, 0, v217, s[46:47]
	v_cndmask_b32_e64 v5, 0, v218, s[46:47]
	v_cndmask_b32_e64 v183, 0, v219, s[46:47]
	v_max3_f32 v157, v157, |v172|, |v174|
	v_max3_f32 v184, v184, |v173|, |v175|
	v_max3_f32 v62, v62, |v158|, |v160|
	v_max3_f32 v34, v34, |v159|, |v161|
	v_max3_f32 v157, v157, |v176|, |v178|
	v_max3_f32 v184, v184, |v177|, |v179|
	v_max3_f32 v62, v62, |v2|, |v4|
	v_max3_f32 v34, v34, |v3|, |v5|
	v_cvt_pkrtz_f16_f32 v5, v5, v183
	v_cvt_pkrtz_f16_f32 v4, v4, v182
	v_cvt_pkrtz_f16_f32 v3, v3, v181
	v_cvt_pkrtz_f16_f32 v2, v2, v180
	v_cvt_pkrtz_f16_f32 v169, v169, v171
	v_cvt_pkrtz_f16_f32 v168, v168, v170
	v_cvt_pkrtz_f16_f32 v167, v166, v167
	v_cvt_pkrtz_f16_f32 v166, v60, v61
	v_max3_f32 v157, v157, |v180|, |v182|
	v_max3_f32 v184, v184, |v181|, |v183|
	v_cvt_pkrtz_f16_f32 v161, v161, v179
	v_cvt_pkrtz_f16_f32 v160, v160, v178
	v_cvt_pkrtz_f16_f32 v159, v159, v177
	v_cvt_pkrtz_f16_f32 v158, v158, v176
	v_cvt_pkrtz_f16_f32 v165, v165, v175
	v_cvt_pkrtz_f16_f32 v164, v164, v174
	v_cvt_pkrtz_f16_f32 v163, v163, v173
	v_cvt_pkrtz_f16_f32 v162, v162, v172
	ds_write_b128 v52, v[166:169]
	ds_write_b128 v53, v[162:165]
	ds_write_b128 v54, v[158:161]
	ds_write_b128 v55, v[2:5]
	ds_bpermute_b32 v2, v56, v62
	ds_bpermute_b32 v3, v56, v157
	ds_bpermute_b32 v4, v56, v34
	ds_bpermute_b32 v5, v56, v184
	s_waitcnt lgkmcnt(0)
	v_max_f32_e32 v2, v2, v2
	v_max_f32_e32 v2, v62, v2
	ds_bpermute_b32 v60, v57, v2
	v_max_f32_e32 v3, v3, v3
	v_max_f32_e32 v3, v157, v3
	v_max_f32_e32 v4, v4, v4
	v_max_f32_e32 v5, v5, v5
	v_max_f32_e32 v4, v34, v4
	v_max_f32_e32 v34, v184, v5
	ds_bpermute_b32 v5, v57, v3
	s_waitcnt lgkmcnt(1)
	v_max_f32_e32 v60, v60, v60
	ds_bpermute_b32 v61, v57, v4
	v_max_f32_e32 v2, v2, v60
	ds_bpermute_b32 v60, v57, v34
	s_waitcnt lgkmcnt(2)
	v_max_f32_e32 v5, v5, v5
	v_max_f32_e32 v5, v3, v5
	s_waitcnt lgkmcnt(1)
	v_max_f32_e32 v3, v61, v61
	v_max_f32_e32 v4, v4, v3
	s_waitcnt lgkmcnt(0)
	v_max_f32_e32 v3, v60, v60
	v_max_f32_e32 v3, v34, v3
	ds_bpermute_b32 v62, v58, v2
	ds_bpermute_b32 v61, v58, v5
	ds_bpermute_b32 v60, v58, v4
	ds_bpermute_b32 v34, v58, v3
	s_and_saveexec_b64 s[46:47], s[6:7]
	s_cbranch_execz .LBB0_33
; #define LAS __attribute__((address_space(3)))
; template <int NCH>
; __device__ __forceinline__ void quant_colblock(const Frame& F, const float* src, int ld_src, int nvalid, unsigned char* dst, int ld_dst, float* sb) {
;     ...
;     for (int sh = 8; sh < 64; sh <<= 1) { m.x = fmaxf(m.x, __shfl_xor(m.x, sh)); m.y = fmaxf(m.y, __shfl_xor(m.y, sh)); m.z = fmaxf(m.z, __shfl_xor(m.z, sh)); m.w = fmaxf(m.w, __shfl_xor(m.w, sh)); }
;     if (kg == 0) *(LAS f32x4*)(cm + w * 32 + n) = m;
	s_waitcnt lgkmcnt(3)
	v_max_f32_e32 v62, v62, v62
	v_max_f32_e32 v2, v2, v2
	v_max_f32_e32 v158, v2, v62
	s_waitcnt lgkmcnt(2)
	v_max_f32_e32 v2, v61, v61
	v_max_f32_e32 v5, v5, v5
	v_max_f32_e32 v159, v5, v2
	s_waitcnt lgkmcnt(1)
	v_max_f32_e32 v2, v60, v60
	v_max_f32_e32 v4, v4, v4
	v_max_f32_e32 v160, v4, v2
	s_waitcnt lgkmcnt(0)
	v_max_f32_e32 v2, v34, v34
	v_max_f32_e32 v3, v3, v3
	v_max_f32_e32 v161, v3, v2
	v_add_u32_e32 v2, s33, v139
	ds_write_b128 v2, v[158:161]

; template <int NCH>
; __device__ __forceinline__ void quant_colblock(const Frame& F, const float* src, int ld_src, int nvalid, unsigned char* dst, int ld_dst, float* sb) {
;     ...
;     for (int bt = 0; bt <= 2 * NCH; ++bt) {
;         if (bt < 2 * NCH) {
; #pragma unroll
;             for (int i = 0; i < 8; ++i) vb[bt & 1][i] = *(const f32x4*)(rb + (size_t)((bt >> 1) * 128 + 8 * (bt & 1) + i) * ld_src + loff); }
;         __builtin_amdgcn_sched_barrier(0);
;         if (bt > 0) { const int pb = bt - 1, c = pb >> 1, hb = pb & 1; f32x4 (&v)[8] = vb[pb & 1]; unsigned t[8][2];
; #pragma unroll
;             for (int i = 0; i < 8; ++i) { v[i].x = ok ? v[i].x : 0.f; v[i].y = ok ? v[i].y : 0.f; v[i].z = ok ? v[i].z : 0.f; v[i].w = ok ? v[i].w : 0.f; }
; #pragma unroll
;             for (int i = 0; i < 8; ++i) { m.x = fmaxf(m.x, fabsf(v[i].x)); m.y = fmaxf(m.y, fabsf(v[i].y)); m.z = fmaxf(m.z, fabsf(v[i].z)); m.w = fmaxf(m.w, fabsf(v[i].w));
; __device__ __forceinline__ void phase_prologue(const Frame& F, const Args& a) {
;     ...
;       if (first >= 0) for (int sblk = first; sblk < NSMALL; sblk += span) { const int b = sblk & 127, hi = sblk >> 7;
;           quant_colblock<2>(F, a.in[10 + hi] + 32 * b, D, 32, ws + (hi ? WS_W_UPN : WS_W_UPP) + (size_t)32 * b * 2048, 2048, (float*)(ws + (hi ? SB_UPN : SB_UPP)) + 32 * b); } }
.LBB0_38:
	s_ashr_i32 s28, s21, 7
	s_ashr_i32 s29, s28, 31
	s_and_b32 s70, s21, 0x7f
	s_lshl_b64 s[28:29], s[28:29], 3
	s_add_u32 s28, s86, s28
	s_addc_u32 s29, s87, s29
	s_load_dwordx2 s[28:29], s[28:29], 0x50
	s_lshl_b32 s30, s70, 7
	s_waitcnt lgkmcnt(0)
	s_add_u32 s28, s28, s30
	s_addc_u32 s29, s29, 0
	s_add_u32 s28, s28, s16
	s_addc_u32 s29, s29, s17
	v_lshl_add_u64 v[122:123], s[28:29], 0, v[132:133]
	v_add_co_u32_e32 v2, vcc, s15, v122
	s_nop 1
	v_addc_co_u32_e32 v3, vcc, 0, v123, vcc
	v_add_co_u32_e32 v6, vcc, s35, v122
	s_nop 1
	v_addc_co_u32_e32 v7, vcc, 0, v123, vcc
	v_add_co_u32_e32 v10, vcc, s36, v122
	global_load_dwordx4 v[2:5], v[2:3], off nt
	s_nop 0
	global_load_dwordx4 v[6:9], v[6:7], off nt
	v_addc_co_u32_e32 v11, vcc, 0, v123, vcc
	v_add_co_u32_e32 v14, vcc, s37, v122
	s_nop 1
	v_addc_co_u32_e32 v15, vcc, 0, v123, vcc
	v_add_co_u32_e32 v18, vcc, s38, v122
	global_load_dwordx4 v[10:13], v[10:11], off nt
	s_nop 0
	global_load_dwordx4 v[14:17], v[14:15], off nt
	v_addc_co_u32_e32 v19, vcc, 0, v123, vcc
	v_add_co_u32_e32 v20, vcc, s39, v122
	s_nop 1
	v_addc_co_u32_e32 v21, vcc, 0, v123, vcc
	v_add_co_u32_e32 v30, vcc, s40, v122
	global_load_dwordx4 v[22:25], v[18:19], off nt
	global_load_dwordx4 v[26:29], v[20:21], off nt
	v_addc_co_u32_e32 v31, vcc, 0, v123, vcc
	global_load_dwordx4 v[18:21], v132, s[28:29] nt
	s_nop 0
	global_load_dwordx4 v[30:33], v[30:31], off nt
	v_add_co_u32_e32 v34, vcc, s41, v122
	s_nop 1
	v_addc_co_u32_e32 v35, vcc, 0, v123, vcc
	v_add_co_u32_e32 v38, vcc, s42, v122
	s_nop 1
	v_addc_co_u32_e32 v39, vcc, 0, v123, vcc
	v_add_co_u32_e32 v42, vcc, s43, v122
	global_load_dwordx4 v[34:37], v[34:35], off nt
	s_nop 0
	global_load_dwordx4 v[38:41], v[38:39], off nt
	v_addc_co_u32_e32 v43, vcc, 0, v123, vcc
	v_add_co_u32_e32 v46, vcc, s44, v122
	s_nop 1
	v_addc_co_u32_e32 v47, vcc, 0, v123, vcc
	v_add_co_u32_e32 v50, vcc, s45, v122
	global_load_dwordx4 v[42:45], v[42:43], off nt
	s_nop 0
	global_load_dwordx4 v[46:49], v[46:47], off nt
	v_addc_co_u32_e32 v51, vcc, 0, v123, vcc
	v_add_co_u32_e32 v54, vcc, s46, v122
	s_nop 1
	v_addc_co_u32_e32 v55, vcc, 0, v123, vcc
	v_add_co_u32_e32 v58, vcc, s47, v122
	global_load_dwordx4 v[50:53], v[50:51], off nt
	s_nop 0
	global_load_dwordx4 v[54:57], v[54:55], off nt
	v_addc_co_u32_e32 v59, vcc, 0, v123, vcc
	v_add_co_u32_e32 v62, vcc, s48, v122
	s_nop 1
	v_addc_co_u32_e32 v63, vcc, 0, v123, vcc
	global_load_dwordx4 v[58:61], v[58:59], off nt
	s_nop 0
	global_load_dwordx4 v[62:65], v[62:63], off nt
	s_waitcnt vmcnt(9)
	v_max3_f32 v66, |v18|, 0, |v2|
	v_max3_f32 v67, |v19|, 0, |v3|
	v_max3_f32 v68, |v20|, 0, |v4|
	v_max3_f32 v69, |v21|, 0, |v5|
	v_max3_f32 v66, v66, |v6|, |v10|
	v_max3_f32 v67, v67, |v7|, |v11|
	v_max3_f32 v68, v68, |v8|, |v12|
	v_max3_f32 v69, v69, |v9|, |v13|
	v_max3_f32 v66, v66, |v14|, |v22|
	v_max3_f32 v67, v67, |v15|, |v23|
	v_max3_f32 v68, v68, |v16|, |v24|
	v_max3_f32 v69, v69, |v17|, |v25|
	s_waitcnt vmcnt(8)
	v_max3_f32 v98, v66, |v26|, |v30|
	v_max3_f32 v99, v67, |v27|, |v31|
	v_max3_f32 v100, v68, |v28|, |v32|
	v_max3_f32 v101, v69, |v29|, |v33|
	v_add_co_u32_e32 v66, vcc, s49, v122
	s_nop 1
	v_addc_co_u32_e32 v67, vcc, 0, v123, vcc
	v_add_co_u32_e32 v70, vcc, s50, v122
	s_nop 1
	v_addc_co_u32_e32 v71, vcc, 0, v123, vcc
	v_add_co_u32_e32 v74, vcc, s51, v122
	global_load_dwordx4 v[66:69], v[66:67], off nt
	s_nop 0
	global_load_dwordx4 v[70:73], v[70:71], off nt
	v_addc_co_u32_e32 v75, vcc, 0, v123, vcc
	v_add_co_u32_e32 v78, vcc, s52, v122
	s_nop 1
	v_addc_co_u32_e32 v79, vcc, 0, v123, vcc
	v_add_co_u32_e32 v82, vcc, s53, v122
	global_load_dwordx4 v[74:77], v[74:75], off nt
	s_nop 0
	global_load_dwordx4 v[78:81], v[78:79], off nt
	v_addc_co_u32_e32 v83, vcc, 0, v123, vcc
	v_add_co_u32_e32 v86, vcc, s54, v122
	s_nop 1
	v_addc_co_u32_e32 v87, vcc, 0, v123, vcc
	v_add_co_u32_e32 v90, vcc, s55, v122
	global_load_dwordx4 v[82:85], v[82:83], off nt
	s_nop 0
	global_load_dwordx4 v[86:89], v[86:87], off nt
	v_addc_co_u32_e32 v91, vcc, 0, v123, vcc
	v_add_co_u32_e32 v94, vcc, s56, v122
	s_nop 1
	v_addc_co_u32_e32 v95, vcc, 0, v123, vcc
	global_load_dwordx4 v[90:93], v[90:91], off nt
	s_nop 0
	global_load_dwordx4 v[94:97], v[94:95], off nt
	s_waitcnt vmcnt(14)
	v_max3_f32 v98, v98, |v34|, |v38|
	v_max3_f32 v99, v99, |v35|, |v39|
	v_max3_f32 v100, v100, |v36|, |v40|
	v_max3_f32 v101, v101, |v37|, |v41|
	s_waitcnt vmcnt(12)
	v_max3_f32 v98, v98, |v42|, |v46|
	v_max3_f32 v99, v99, |v43|, |v47|
	v_max3_f32 v100, v100, |v44|, |v48|
	v_max3_f32 v101, v101, |v45|, |v49|
	s_waitcnt vmcnt(10)
; #define LAS __attribute__((address_space(3)))
; template <int NCH>
; __device__ __forceinline__ void quant_colblock(const Frame& F, const float* src, int ld_src, int nvalid, unsigned char* dst, int ld_dst, float* sb) {
;     ...
;             for (int i = 0; i < 8; ++i) { m.x = fmaxf(m.x, fabsf(v[i].x)); m.y = fmaxf(m.y, fabsf(v[i].y)); m.z = fmaxf(m.z, fabsf(v[i].z)); m.w = fmaxf(m.w, fabsf(v[i].w));
;                 t[i][0] = __builtin_bit_cast(unsigned, __builtin_amdgcn_cvt_pkrtz(v[i].x, v[i].y)); t[i][1] = __builtin_bit_cast(unsigned, __builtin_amdgcn_cvt_pkrtz(v[i].z, v[i].w)); }
;             if (c < NREG) {
; #pragma unroll
;                 for (int i = 0; i < 8; ++i) { h[c < NREG ? c : 0][8 * hb + i][0] = t[i][0]; h[c < NREG ? c : 0][8 * hb + i][1] = t[i][1]; } }
;             else {
; #pragma unroll
;                 for (int e = 0; e < 4; ++e) hl[((c - 2) * 8 + 4 * hb + e) * 512] = (u32x4){t[2 * e][0], t[2 * e][1], t[2 * e + 1][0], t[2 * e + 1][1]}; }
;             __builtin_amdgcn_sched_barrier(0); } }
; #pragma unroll
;     for (int sh = 8; sh < 64; sh <<= 1) { m.x = fmaxf(m.x, __shfl_xor(m.x, sh)); m.y = fmaxf(m.y, __shfl_xor(m.y, sh)); m.z = fmaxf(m.z, __shfl_xor(m.z, sh)); m.w = fmaxf(m.w, __shfl_xor(m.w, sh)); }
;     if (kg == 0) *(LAS f32x4*)(cm + w * 32 + n) = m;
	v_max3_f32 v98, v98, |v50|, |v54|
	v_max3_f32 v99, v99, |v51|, |v55|
	v_max3_f32 v100, v100, |v52|, |v56|
	v_max3_f32 v101, v101, |v53|, |v57|
	s_waitcnt vmcnt(8)
	v_max3_f32 v134, v98, |v58|, |v62|
	v_max3_f32 v135, v99, |v59|, |v63|
	v_max3_f32 v136, v100, |v60|, |v64|
	v_max3_f32 v137, v101, |v61|, |v65|
	v_add_co_u32_e32 v98, vcc, s57, v122
	s_nop 1
	v_addc_co_u32_e32 v99, vcc, 0, v123, vcc
	v_add_co_u32_e32 v102, vcc, s58, v122
	s_nop 1
	v_addc_co_u32_e32 v103, vcc, 0, v123, vcc
	v_add_co_u32_e32 v106, vcc, s59, v122
	global_load_dwordx4 v[98:101], v[98:99], off nt
	s_nop 0
	global_load_dwordx4 v[102:105], v[102:103], off nt
	v_addc_co_u32_e32 v107, vcc, 0, v123, vcc
	v_add_co_u32_e32 v110, vcc, s60, v122
	s_nop 1
	v_addc_co_u32_e32 v111, vcc, 0, v123, vcc
	v_add_co_u32_e32 v114, vcc, s61, v122
	global_load_dwordx4 v[106:109], v[106:107], off nt
	s_nop 0
	global_load_dwordx4 v[110:113], v[110:111], off nt
	v_addc_co_u32_e32 v115, vcc, 0, v123, vcc
	v_add_co_u32_e32 v118, vcc, s62, v122
	s_nop 1
	v_addc_co_u32_e32 v119, vcc, 0, v123, vcc
	v_add_co_u32_e32 v124, vcc, s63, v122
	global_load_dwordx4 v[114:117], v[114:115], off nt
	s_nop 0
	global_load_dwordx4 v[118:121], v[118:119], off nt
	v_addc_co_u32_e32 v125, vcc, 0, v123, vcc
	v_add_co_u32_e32 v126, vcc, s64, v122
	s_nop 1
	v_addc_co_u32_e32 v127, vcc, 0, v123, vcc
	global_load_dwordx4 v[122:125], v[124:125], off nt
	s_nop 0
	global_load_dwordx4 v[126:129], v[126:127], off nt
	s_waitcnt vmcnt(14)
	v_max3_f32 v134, v134, |v66|, |v70|
	v_max3_f32 v135, v135, |v67|, |v71|
	v_max3_f32 v136, v136, |v68|, |v72|
	v_max3_f32 v137, v137, |v69|, |v73|
	s_waitcnt vmcnt(12)
	v_max3_f32 v134, v134, |v74|, |v78|
	v_max3_f32 v135, v135, |v75|, |v79|
	v_max3_f32 v136, v136, |v76|, |v80|
	v_max3_f32 v137, v137, |v77|, |v81|
	s_waitcnt vmcnt(10)
	v_max3_f32 v134, v134, |v82|, |v86|
	v_max3_f32 v135, v135, |v83|, |v87|
	v_max3_f32 v136, v136, |v84|, |v88|
	v_max3_f32 v137, v137, |v85|, |v89|
	s_waitcnt vmcnt(8)
	v_max3_f32 v134, v134, |v90|, |v94|
	v_max3_f32 v135, v135, |v91|, |v95|
	v_max3_f32 v136, v136, |v92|, |v96|
	v_max3_f32 v137, v137, |v93|, |v97|
	s_waitcnt vmcnt(6)
	v_max3_f32 v134, v134, |v98|, |v102|
	s_waitcnt vmcnt(4)
	v_max3_f32 v134, v134, |v106|, |v110|
	v_max3_f32 v135, v135, |v99|, |v103|
	s_waitcnt vmcnt(2)
	v_max3_f32 v134, v134, |v114|, |v118|
	v_max3_f32 v135, v135, |v107|, |v111|
	s_waitcnt vmcnt(0)
	v_max3_f32 v134, v134, |v122|, |v126|
	v_max3_f32 v135, v135, |v115|, |v119|
	v_max3_f32 v136, v136, |v100|, |v104|
	v_max3_f32 v135, v135, |v123|, |v127|
	v_max3_f32 v136, v136, |v108|, |v112|
	ds_bpermute_b32 v143, v140, v134
	v_max3_f32 v136, v136, |v116|, |v120|
	ds_bpermute_b32 v144, v140, v135
	v_max3_f32 v136, v136, |v124|, |v128|
	v_max3_f32 v137, v137, |v101|, |v105|
	v_max3_f32 v137, v137, |v109|, |v113|
	ds_bpermute_b32 v145, v140, v136
	v_max3_f32 v137, v137, |v117|, |v121|
	v_max3_f32 v137, v137, |v125|, |v129|
	s_waitcnt lgkmcnt(2)
	v_max_f32_e32 v143, v143, v143
	v_max_f32_e32 v134, v134, v143
	s_waitcnt lgkmcnt(1)
	v_max_f32_e32 v143, v144, v144
	ds_bpermute_b32 v144, v140, v137
	v_max_f32_e32 v135, v135, v143
	s_waitcnt lgkmcnt(1)
	v_max_f32_e32 v143, v145, v145
	ds_bpermute_b32 v145, v141, v134
	v_max_f32_e32 v136, v136, v143
	s_waitcnt lgkmcnt(1)
	v_max_f32_e32 v143, v144, v144
	v_max_f32_e32 v143, v137, v143
	ds_bpermute_b32 v137, v141, v135
	s_waitcnt lgkmcnt(1)
	v_max_f32_e32 v144, v145, v145
	ds_bpermute_b32 v145, v141, v136
	v_max_f32_e32 v134, v134, v144
	ds_bpermute_b32 v144, v141, v143
	s_waitcnt lgkmcnt(2)
	v_max_f32_e32 v137, v137, v137
	v_max_f32_e32 v137, v135, v137
	s_waitcnt lgkmcnt(1)
	v_max_f32_e32 v135, v145, v145
	v_max_f32_e32 v136, v136, v135
	s_waitcnt lgkmcnt(0)
	v_max_f32_e32 v135, v144, v144
	v_max_f32_e32 v135, v143, v135
	ds_bpermute_b32 v146, v142, v134
	ds_bpermute_b32 v145, v142, v137
	ds_bpermute_b32 v144, v142, v136
	ds_bpermute_b32 v143, v142, v135
	s_and_saveexec_b64 s[28:29], s[6:7]
	s_cbranch_execz .LBB0_40
	s_waitcnt lgkmcnt(3)
	v_max_f32_e32 v146, v146, v146
	v_max_f32_e32 v134, v134, v134
	v_max_f32_e32 v146, v134, v146
	s_waitcnt lgkmcnt(2)
	v_max_f32_e32 v134, v145, v145
	v_max_f32_e32 v137, v137, v137
	v_max_f32_e32 v147, v137, v134
	s_waitcnt lgkmcnt(1)
	v_max_f32_e32 v134, v144, v144
	v_max_f32_e32 v136, v136, v136
	v_max_f32_e32 v148, v136, v134
	s_waitcnt lgkmcnt(0)
	v_max_f32_e32 v134, v143, v143
	v_max_f32_e32 v135, v135, v135
	v_max_f32_e32 v149, v135, v134
	v_add_u32_e32 v134, s33, v139
	ds_write_b128 v134, v[146:149]
